# P3..P5 conversion stream: a stopped wave skips the pipelined reload of its current item (waits vmcnt(0) instead, so the loop's counted waits stay met)
# speedup vs baseline: 1.0111x; 1.0021x over previous
; __device__ __forceinline__ void t128_load(const float* W, int N, int item, int lane, f32x4 (&v)[16]) {
;     const int nblk = N / 32, kb = item / nblk, nb = item % nblk, k0 = 128 * kb, n0 = 32 * nb;
; #pragma unroll
;     for (int i = 0; i < 16; ++i) v[i] = __builtin_nontemporal_load((const f32x4*)(W + (size_t)(k0 + i * 8 + (lane >> 3)) * N + n0 + (lane & 7) * 4));
; }
; __device__ __forceinline__ int conv_stream(const Ctx& c, int j, int first, int step, const unsigned* stop, const float* w_gu, const float* w_d, unsigned char* Wgu, unsigned char* Wd) {
;     ...
;         { const int i2 = i + step; const bool more = j + CONV_SLOTS * i2 < CONV_TOTAL && !(stop && stop_poll(c, stop) >= STOP_AT);
;           cs_load(j + CONV_SLOTS * (more ? i2 : i), c.lane, w_gu, w_d, vb);
;           cs_store(c, j + CONV_SLOTS * i, va, Wgu, Wd); i = i2; if (!more) break; }
;         { const int i2 = i + step; const bool more = j + CONV_SLOTS * i2 < CONV_TOTAL && !(stop && stop_poll(c, stop) >= STOP_AT);
;           cs_load(j + CONV_SLOTS * (more ? i2 : i), c.lane, w_gu, w_d, va);
;           cs_store(c, j + CONV_SLOTS * i, vb, Wgu, Wd); i = i2; if (!more) break; }
.LBB0_672:
	s_waitcnt vmcnt(4)
	v_or_b32_e32 v122, s21, v131
	v_ashrrev_i32_e32 v123, 31, v122
	v_lshlrev_b64 v[66:67], s58, v[122:123]
	v_add_u32_e32 v68, 8, v122
	v_add_u32_e32 v74, 16, v122
	v_add_u32_e32 v76, 24, v122
	v_add_u32_e32 v82, 32, v122
	v_add_u32_e32 v84, 40, v122
	v_add_u32_e32 v90, 48, v122
	v_add_u32_e32 v92, 56, v122
	v_add_u32_e32 v98, 64, v122
	v_add_u32_e32 v100, 0x48, v122
	v_add_u32_e32 v106, 0x50, v122
	v_add_u32_e32 v108, 0x58, v122
	v_add_u32_e32 v114, 0x60, v122
	v_add_u32_e32 v116, 0x68, v122
	v_add_u32_e32 v126, 0x70, v122
	v_add_u32_e32 v122, 0x78, v122
	v_lshlrev_b32_e32 v132, 2, v130
	v_ashrrev_i32_e32 v69, 31, v68
	v_ashrrev_i32_e32 v75, 31, v74
	v_ashrrev_i32_e32 v77, 31, v76
	v_ashrrev_i32_e32 v83, 31, v82
	v_ashrrev_i32_e32 v85, 31, v84
	v_ashrrev_i32_e32 v91, 31, v90
	v_ashrrev_i32_e32 v93, 31, v92
	v_ashrrev_i32_e32 v99, 31, v98
	v_ashrrev_i32_e32 v101, 31, v100
	v_ashrrev_i32_e32 v107, 31, v106
	v_ashrrev_i32_e32 v109, 31, v108
	v_ashrrev_i32_e32 v115, 31, v114
	v_ashrrev_i32_e32 v117, 31, v116
	v_ashrrev_i32_e32 v127, 31, v126
	v_ashrrev_i32_e32 v123, 31, v122
	v_lshl_add_u64 v[124:125], s[60:61], 0, v[132:133]
	v_lshlrev_b64 v[68:69], s58, v[68:69]
	v_lshlrev_b64 v[74:75], s58, v[74:75]
	v_lshlrev_b64 v[76:77], s58, v[76:77]
	v_lshlrev_b64 v[82:83], s58, v[82:83]
	v_lshlrev_b64 v[84:85], s58, v[84:85]
	v_lshlrev_b64 v[90:91], s58, v[90:91]
	v_lshlrev_b64 v[92:93], s58, v[92:93]
	v_lshlrev_b64 v[98:99], s58, v[98:99]
	v_lshlrev_b64 v[100:101], s58, v[100:101]
	v_lshlrev_b64 v[106:107], s58, v[106:107]
	v_lshlrev_b64 v[108:109], s58, v[108:109]
	v_lshlrev_b64 v[114:115], s58, v[114:115]
	v_lshlrev_b64 v[116:117], s58, v[116:117]
	v_lshlrev_b64 v[126:127], s58, v[126:127]
	v_lshlrev_b64 v[122:123], s58, v[122:123]
	v_lshl_add_u64 v[66:67], v[124:125], 0, v[66:67]
	v_lshl_add_u64 v[68:69], v[124:125], 0, v[68:69]
	v_lshl_add_u64 v[74:75], v[124:125], 0, v[74:75]
	v_lshl_add_u64 v[76:77], v[124:125], 0, v[76:77]
	v_lshl_add_u64 v[82:83], v[124:125], 0, v[82:83]
	v_lshl_add_u64 v[84:85], v[124:125], 0, v[84:85]
	v_lshl_add_u64 v[90:91], v[124:125], 0, v[90:91]
	v_lshl_add_u64 v[92:93], v[124:125], 0, v[92:93]
	v_lshl_add_u64 v[98:99], v[124:125], 0, v[98:99]
	v_lshl_add_u64 v[100:101], v[124:125], 0, v[100:101]
	v_lshl_add_u64 v[106:107], v[124:125], 0, v[106:107]
	v_lshl_add_u64 v[108:109], v[124:125], 0, v[108:109]
	v_lshl_add_u64 v[114:115], v[124:125], 0, v[114:115]
	v_lshl_add_u64 v[116:117], v[124:125], 0, v[116:117]
	v_lshl_add_u64 v[126:127], v[124:125], 0, v[126:127]
	v_lshl_add_u64 v[122:123], v[124:125], 0, v[122:123]
	s_and_b64 vcc, exec, s[56:57]
	s_cbranch_vccnz .Lcv3a_load
	s_waitcnt vmcnt(0)
	s_branch .Lcv3a_noload
.Lcv3a_load:
	global_load_dwordx4 v[70:73], v[66:67], off nt
	s_nop 0
	global_load_dwordx4 v[66:69], v[68:69], off nt
	s_nop 0
	global_load_dwordx4 v[78:81], v[74:75], off nt
	s_nop 0
	global_load_dwordx4 v[74:77], v[76:77], off nt
	s_nop 0
	global_load_dwordx4 v[86:89], v[82:83], off nt
	s_nop 0
	global_load_dwordx4 v[82:85], v[84:85], off nt
	s_nop 0
	global_load_dwordx4 v[94:97], v[90:91], off nt
	s_nop 0
	global_load_dwordx4 v[90:93], v[92:93], off nt
	s_nop 0
	global_load_dwordx4 v[102:105], v[98:99], off nt
	s_nop 0
	global_load_dwordx4 v[98:101], v[100:101], off nt
	s_nop 0
	global_load_dwordx4 v[110:113], v[106:107], off nt
	s_nop 0
	global_load_dwordx4 v[106:109], v[108:109], off nt
	s_nop 0
	global_load_dwordx4 v[118:121], v[114:115], off nt
	s_nop 0
	global_load_dwordx4 v[114:117], v[116:117], off nt
	s_nop 0
	global_load_dwordx4 v[126:129], v[126:127], off nt
	s_nop 0
	global_load_dwordx4 v[122:125], v[122:123], off nt
.Lcv3a_noload:
	s_add_i32 s28, s25, 0xfffff800
	s_mov_b64 s[58:59], -1
	s_cmpk_gt_i32 s28, 0x7fff
	v_add_u32_e32 v154, 0x1080, v144
	v_add_u32_e32 v155, 0x1088, v144
	v_add_u32_e32 v156, 0x14a0, v144
	v_add_u32_e32 v157, 0x14a8, v144
	v_add_u32_e32 v158, 0x18c0, v144
	v_add_u32_e32 v159, 0x18c8, v144
	v_add_u32_e32 v160, 0x1ce0, v144
	v_add_u32_e32 v161, 0x1ce8, v144
	v_add_u32_e32 v162, 0x2100, v144
	v_add_u32_e32 v163, 0x2108, v144
	v_add_u32_e32 v164, 0x2520, v144
	v_add_u32_e32 v165, 0x2528, v144
	v_add_u32_e32 v166, 0x2940, v144
	v_add_u32_e32 v167, 0x2948, v144
	v_add_u32_e32 v168, 0x2d60, v144
	v_add_u32_e32 v169, 0x2d68, v144
	v_add_u32_e32 v170, 0x3180, v144
	v_add_u32_e32 v171, 0x3188, v144
	v_add_u32_e32 v172, 0x35a0, v144
	v_add_u32_e32 v173, 0x35a8, v144
	v_add_u32_e32 v174, 0x39c0, v144
	v_add_u32_e32 v175, 0x39c8, v144
	v_add_u32_e32 v176, 0x3de0, v144
	v_add_u32_e32 v177, 0x3de8, v144
	v_add_u32_e32 v153, 0x400, v148
	v_add_u32_e32 v152, 0x600, v148
	s_cbranch_scc0 .LBB0_691
; #define LAS __attribute__((address_space(3)))
; #define LDS_WAIT() asm volatile("s_waitcnt lgkmcnt(0)" ::: "memory")
; template <int MODE>
; __device__ __forceinline__ void t128_store(const Ctx& c, const f32x4 (&v)[16], int K, int N, unsigned char* WT, int item) {
;     LAS float* scr = (LAS float*)(c.lds + c.wave * CONV_SCR);
;     const int nblk = N / 32, kb = item / nblk, nb = item % nblk, k0 = 128 * kb, n0 = 32 * nb, lane = c.lane;
; #pragma unroll
;     for (int i = 0; i < 16; ++i) { LAS float* d = scr + (i * 8 + (lane >> 3)) * 33 + (lane & 7) * 4; d[0] = v[i].x; d[1] = v[i].y; d[2] = v[i].z; d[3] = v[i].w; }
;     LDS_WAIT(); asm volatile("" ::: "memory");
;     const int cc = lane & 7;
; #pragma unroll
;     for (int j = 0; j < 4; ++j) { const int n = (lane >> 3) + 8 * j; const LAS float* s = scr + (16 * cc) * 33 + n; int w[4];
; #pragma unroll
;         for (int q = 0; q < 4; ++q) { int t = 0; t = __builtin_amdgcn_cvt_pk_fp8_f32(s[(4 * q) * 33] * WSCALE, s[(4 * q + 1) * 33] * WSCALE, t, false);
;             t = __builtin_amdgcn_cvt_pk_fp8_f32(s[(4 * q + 2) * 33] * WSCALE, s[(4 * q + 3) * 33] * WSCALE, t, true); w[q] = t; }
;         const int dr = drow_of<MODE>(n0 + n);
;         __builtin_nontemporal_store((u32x4){(unsigned)w[0], (unsigned)w[1], (unsigned)w[2], (unsigned)w[3]}, (u32x4*)(WT + (size_t)dr * K + k0 + 16 * cc)); }
;     LDS_WAIT(); asm volatile("" ::: "memory");
; }
; __device__ __forceinline__ void cs_store(const Ctx& c, int it, const f32x4 (&v)[16], unsigned char* Wgu, unsigned char* Wd) {
;     if (it < I_D) { constexpr int per = (DFF / 128) * (D / 32); t128_store<0>(c, v, DFF, D, Wd + (size_t)(it / per) * D * DFF, it % per); }
;     else { const int r = it - I_D; constexpr int per = (D / 128) * (4096 / 32); t128_store<1>(c, v, D, 4096, Wgu + (size_t)(r / per) * 4096 * D, r % per); }
	s_waitcnt vmcnt(31)
	ds_write2_b32 v144, v6, v7 offset1:1
	ds_write2_b32 v144, v8, v9 offset0:2 offset1:3
	s_waitcnt vmcnt(30)
	ds_write2_b32 v149, v2, v3 offset1:1
	ds_write2_b32 v149, v4, v5 offset0:2 offset1:3
	s_waitcnt vmcnt(29)
	ds_write2_b32 v150, v14, v15 offset1:1
	ds_write2_b32 v150, v16, v17 offset0:2 offset1:3
	s_waitcnt vmcnt(28)
	ds_write2_b32 v151, v10, v11 offset1:1
	ds_write2_b32 v151, v12, v13 offset0:2 offset1:3
	s_waitcnt vmcnt(27)
	ds_write2_b32 v154, v22, v23 offset1:1
	ds_write2_b32 v155, v24, v25 offset1:1
	s_waitcnt vmcnt(26)
	ds_write2_b32 v156, v18, v19 offset1:1
	ds_write2_b32 v157, v20, v21 offset1:1
	s_waitcnt vmcnt(25)
	ds_write2_b32 v158, v30, v31 offset1:1
	ds_write2_b32 v159, v32, v33 offset1:1
	s_waitcnt vmcnt(24)
	ds_write2_b32 v160, v26, v27 offset1:1
	ds_write2_b32 v161, v28, v29 offset1:1
	s_waitcnt vmcnt(23)
	ds_write2_b32 v162, v38, v39 offset1:1
	ds_write2_b32 v163, v40, v41 offset1:1
	s_waitcnt vmcnt(22)
	ds_write2_b32 v164, v34, v35 offset1:1
	ds_write2_b32 v165, v36, v37 offset1:1
	s_waitcnt vmcnt(21)
	ds_write2_b32 v166, v46, v47 offset1:1
	ds_write2_b32 v167, v48, v49 offset1:1
	s_waitcnt vmcnt(20)
	ds_write2_b32 v168, v42, v43 offset1:1
	ds_write2_b32 v169, v44, v45 offset1:1
	s_waitcnt vmcnt(19)
	ds_write2_b32 v170, v54, v55 offset1:1
	ds_write2_b32 v171, v56, v57 offset1:1
	s_waitcnt vmcnt(18)
	ds_write2_b32 v172, v50, v51 offset1:1
	ds_write2_b32 v173, v52, v53 offset1:1
	s_waitcnt vmcnt(17)
	ds_write2_b32 v174, v62, v63 offset1:1
	ds_write2_b32 v175, v64, v65 offset1:1
	s_waitcnt vmcnt(16)
	ds_write2_b32 v176, v58, v59 offset1:1
	ds_write2_b32 v177, v60, v61 offset1:1
	s_waitcnt lgkmcnt(0)
	ds_read2_b32 v[182:183], v148 offset1:8
	ds_read2_b32 v[184:185], v148 offset0:33 offset1:41
	ds_read2_b32 v[188:189], v148 offset0:66 offset1:74
	ds_read2_b32 v[190:191], v148 offset0:99 offset1:107
	v_mov_b32_e32 v178, v133
	ds_read2_b32 v[192:193], v148 offset0:132 offset1:140
	ds_read2_b32 v[194:195], v148 offset0:165 offset1:173
	s_waitcnt lgkmcnt(5)
	v_mul_f32_e32 v179, 0x42800000, v182
	s_waitcnt lgkmcnt(4)
	v_mul_f32_e32 v180, 0x42800000, v184
	v_cvt_pk_fp8_f32 v178, v179, v180
	s_waitcnt lgkmcnt(3)
	v_mul_f32_e32 v179, 0x42800000, v188
	s_waitcnt lgkmcnt(2)
	v_mul_f32_e32 v180, 0x42800000, v190
	ds_read2_b32 v[196:197], v148 offset0:198 offset1:206
	ds_read2_b32 v[198:199], v148 offset0:231 offset1:239
	v_cvt_pk_fp8_f32 v178, v179, v180 op_sel:[0,0,1]
	s_waitcnt lgkmcnt(3)
	v_mul_f32_e32 v180, 0x42800000, v192
	s_waitcnt lgkmcnt(2)
	v_mul_f32_e32 v181, 0x42800000, v194
	v_mov_b32_e32 v179, v133
	ds_read2_b32 v[200:201], v153 offset0:8 offset1:16
	ds_read2_b32 v[202:203], v153 offset0:41 offset1:49
	v_cvt_pk_fp8_f32 v179, v180, v181
	ds_read2_b32 v[204:205], v153 offset0:74 offset1:82
	ds_read2_b32 v[206:207], v153 offset0:107 offset1:115
	ds_read2_b32 v[208:209], v153 offset0:140 offset1:148
	ds_read2_b32 v[210:211], v153 offset0:173 offset1:181
	s_waitcnt lgkmcnt(7)
	v_mul_f32_e32 v180, 0x42800000, v196
	s_waitcnt lgkmcnt(6)
	v_mul_f32_e32 v181, 0x42800000, v198
	v_cvt_pk_fp8_f32 v179, v180, v181 op_sel:[0,0,1]
	s_waitcnt lgkmcnt(5)
	v_mul_f32_e32 v181, 0x42800000, v200
	s_waitcnt lgkmcnt(4)
	v_mul_f32_e32 v182, 0x42800000, v202
	v_mov_b32_e32 v180, v133
	ds_read2_b32 v[212:213], v153 offset0:206 offset1:214
	ds_read2_b32 v[214:215], v153 offset0:239 offset1:247
	v_cvt_pk_fp8_f32 v180, v181, v182
	s_waitcnt lgkmcnt(3)
	v_mul_f32_e32 v188, 0x42800000, v208
	s_waitcnt lgkmcnt(2)
	v_mul_f32_e32 v190, 0x42800000, v210
	v_mov_b32_e32 v181, v133
	v_cvt_pk_fp8_f32 v181, v188, v190
	v_mul_f32_e32 v182, 0x42800000, v204
	v_mul_f32_e32 v184, 0x42800000, v206
	v_cvt_pk_fp8_f32 v180, v182, v184 op_sel:[0,0,1]
	s_waitcnt lgkmcnt(1)
	v_mul_f32_e32 v182, 0x42800000, v212
	s_waitcnt lgkmcnt(0)
; #define LAS __attribute__((address_space(3)))
; #define LDS_WAIT() asm volatile("s_waitcnt lgkmcnt(0)" ::: "memory")
; template <int MODE>
; __device__ __forceinline__ void t128_store(const Ctx& c, const f32x4 (&v)[16], int K, int N, unsigned char* WT, int item) {
;     LAS float* scr = (LAS float*)(c.lds + c.wave * CONV_SCR);
;     const int nblk = N / 32, kb = item / nblk, nb = item % nblk, k0 = 128 * kb, n0 = 32 * nb, lane = c.lane;
; #pragma unroll
;     for (int i = 0; i < 16; ++i) { LAS float* d = scr + (i * 8 + (lane >> 3)) * 33 + (lane & 7) * 4; d[0] = v[i].x; d[1] = v[i].y; d[2] = v[i].z; d[3] = v[i].w; }
;     LDS_WAIT(); asm volatile("" ::: "memory");
;     const int cc = lane & 7;
; #pragma unroll
;     for (int j = 0; j < 4; ++j) { const int n = (lane >> 3) + 8 * j; const LAS float* s = scr + (16 * cc) * 33 + n; int w[4];
; #pragma unroll
;         for (int q = 0; q < 4; ++q) { int t = 0; t = __builtin_amdgcn_cvt_pk_fp8_f32(s[(4 * q) * 33] * WSCALE, s[(4 * q + 1) * 33] * WSCALE, t, false);
;             t = __builtin_amdgcn_cvt_pk_fp8_f32(s[(4 * q + 2) * 33] * WSCALE, s[(4 * q + 3) * 33] * WSCALE, t, true); w[q] = t; }
;         const int dr = drow_of<MODE>(n0 + n);
;         __builtin_nontemporal_store((u32x4){(unsigned)w[0], (unsigned)w[1], (unsigned)w[2], (unsigned)w[3]}, (u32x4*)(WT + (size_t)dr * K + k0 + 16 * cc)); }
;     LDS_WAIT(); asm volatile("" ::: "memory");
; }
; __device__ __forceinline__ void cs_store(const Ctx& c, int it, const f32x4 (&v)[16], unsigned char* Wgu, unsigned char* Wd) {
;     if (it < I_D) { constexpr int per = (DFF / 128) * (D / 32); t128_store<0>(c, v, DFF, D, Wd + (size_t)(it / per) * D * DFF, it % per); }
;     else { const int r = it - I_D; constexpr int per = (D / 128) * (4096 / 32); t128_store<1>(c, v, D, 4096, Wgu + (size_t)(r / per) * 4096 * D, r % per); }
	v_mul_f32_e32 v184, 0x42800000, v214
	v_cvt_pk_fp8_f32 v181, v182, v184 op_sel:[0,0,1]
	v_mul_f32_e32 v183, 0x42800000, v183
	v_mul_f32_e32 v184, 0x42800000, v185
	v_mov_b32_e32 v182, v133
	v_cvt_pk_fp8_f32 v182, v183, v184
	v_mul_f32_e32 v184, 0x42800000, v189
	v_mul_f32_e32 v188, 0x42800000, v193
	v_mul_f32_e32 v189, 0x42800000, v195
	v_mov_b32_e32 v183, v133
	v_cvt_pk_fp8_f32 v183, v188, v189
	v_mul_f32_e32 v185, 0x42800000, v191
	v_cvt_pk_fp8_f32 v182, v184, v185 op_sel:[0,0,1]
	v_mul_f32_e32 v184, 0x42800000, v197
	v_mul_f32_e32 v185, 0x42800000, v199
	s_add_i32 s20, s25, 0xffff7800
	v_cvt_pk_fp8_f32 v183, v184, v185 op_sel:[0,0,1]
	v_mul_f32_e32 v185, 0x42800000, v201
	v_mul_f32_e32 v188, 0x42800000, v203
	v_mov_b32_e32 v184, v133
	s_lshr_b32 s54, s20, 11
	v_cvt_pk_fp8_f32 v184, v185, v188
	v_mul_f32_e32 v190, 0x42800000, v209
	v_mul_f32_e32 v191, 0x42800000, v211
	v_mov_b32_e32 v185, v133
	s_lshl_b64 s[20:21], s[54:55], 23
	v_cvt_pk_fp8_f32 v185, v190, v191
	s_add_u32 s20, s14, s20
	s_addc_u32 s21, s15, s21
	s_and_b32 s29, s28, 0x780
	v_mul_f32_e32 v188, 0x42800000, v205
	v_mul_f32_e32 v189, 0x42800000, v207
	s_add_u32 s20, s20, s29
	v_cvt_pk_fp8_f32 v184, v188, v189 op_sel:[0,0,1]
	v_mul_f32_e32 v188, 0x42800000, v213
	v_mul_f32_e32 v189, 0x42800000, v215
	s_addc_u32 s21, s21, 0
	v_cvt_pk_fp8_f32 v185, v188, v189 op_sel:[0,0,1]
	v_lshl_add_u64 v[186:187], s[20:21], 0, v[134:135]
	ds_read2_b32 v[188:189], v148 offset0:16 offset1:24
	ds_read2_b32 v[190:191], v148 offset0:49 offset1:57
	v_lshl_add_u64 v[216:217], v[186:187], 0, v[136:137]
	global_store_dwordx4 v[216:217], v[178:181], off nt
	s_nop 1
	v_lshl_add_u64 v[178:179], v[186:187], 0, v[138:139]
	global_store_dwordx4 v[178:179], v[182:185], off nt
	ds_read2_b32 v[182:183], v148 offset0:82 offset1:90
	ds_read2_b32 v[184:185], v148 offset0:115 offset1:123
	s_waitcnt lgkmcnt(3)
	v_mul_f32_e32 v179, 0x42800000, v188
	s_waitcnt lgkmcnt(2)
	v_mul_f32_e32 v180, 0x42800000, v190
	v_mov_b32_e32 v178, v133
	ds_read2_b32 v[192:193], v148 offset0:148 offset1:156
	ds_read2_b32 v[194:195], v148 offset0:181 offset1:189
	v_cvt_pk_fp8_f32 v178, v179, v180
	s_waitcnt lgkmcnt(3)
	v_mul_f32_e32 v179, 0x42800000, v182
	s_waitcnt lgkmcnt(2)
	v_mul_f32_e32 v180, 0x42800000, v184
	ds_read2_b32 v[196:197], v148 offset0:214 offset1:222
	ds_read2_b32 v[198:199], v148 offset0:247 offset1:255
	v_cvt_pk_fp8_f32 v178, v179, v180 op_sel:[0,0,1]
	s_waitcnt lgkmcnt(3)
	v_mul_f32_e32 v180, 0x42800000, v192
	s_waitcnt lgkmcnt(2)
	v_mul_f32_e32 v181, 0x42800000, v194
	v_mov_b32_e32 v179, v133
	ds_read2_b32 v[200:201], v153 offset0:24 offset1:32
	ds_read2_b32 v[202:203], v153 offset0:57 offset1:65
	v_cvt_pk_fp8_f32 v179, v180, v181
	ds_read2_b32 v[204:205], v153 offset0:90 offset1:98
	ds_read2_b32 v[206:207], v153 offset0:123 offset1:131
	ds_read2_b32 v[208:209], v153 offset0:156 offset1:164
	ds_read2_b32 v[210:211], v153 offset0:189 offset1:197
	s_waitcnt lgkmcnt(7)
	v_mul_f32_e32 v180, 0x42800000, v196
	s_waitcnt lgkmcnt(6)
	v_mul_f32_e32 v181, 0x42800000, v198
	v_cvt_pk_fp8_f32 v179, v180, v181 op_sel:[0,0,1]
	s_waitcnt lgkmcnt(5)
	v_mul_f32_e32 v181, 0x42800000, v200
	s_waitcnt lgkmcnt(4)
	v_mul_f32_e32 v182, 0x42800000, v202
	v_mov_b32_e32 v180, v133
	ds_read2_b32 v[212:213], v153 offset0:222 offset1:230
	ds_read2_b32 v[214:215], v152 offset0:127 offset1:135
	v_cvt_pk_fp8_f32 v180, v181, v182
	s_waitcnt lgkmcnt(3)
	v_mul_f32_e32 v188, 0x42800000, v208
	s_waitcnt lgkmcnt(2)
	v_mul_f32_e32 v190, 0x42800000, v210
	v_mov_b32_e32 v181, v133
	v_cvt_pk_fp8_f32 v181, v188, v190
	v_mul_f32_e32 v182, 0x42800000, v204
	v_mul_f32_e32 v184, 0x42800000, v206
	v_cvt_pk_fp8_f32 v180, v182, v184 op_sel:[0,0,1]
	s_waitcnt lgkmcnt(1)
	v_mul_f32_e32 v182, 0x42800000, v212
	s_waitcnt lgkmcnt(0)
	v_mul_f32_e32 v184, 0x42800000, v214
	v_cvt_pk_fp8_f32 v181, v182, v184 op_sel:[0,0,1]
	v_mul_f32_e32 v184, 0x42800000, v189
	v_mul_f32_e32 v188, 0x42800000, v191
	v_mov_b32_e32 v182, v133
	v_cvt_pk_fp8_f32 v182, v184, v188
	v_mul_f32_e32 v184, 0x42800000, v183
	v_mul_f32_e32 v188, 0x42800000, v193
	v_mul_f32_e32 v189, 0x42800000, v195
	v_mov_b32_e32 v183, v133
	v_cvt_pk_fp8_f32 v183, v188, v189
	v_mul_f32_e32 v185, 0x42800000, v185
	v_cvt_pk_fp8_f32 v182, v184, v185 op_sel:[0,0,1]
	v_mul_f32_e32 v184, 0x42800000, v197
	v_mul_f32_e32 v185, 0x42800000, v199
	v_cvt_pk_fp8_f32 v183, v184, v185 op_sel:[0,0,1]
	v_mul_f32_e32 v185, 0x42800000, v201
	v_mul_f32_e32 v188, 0x42800000, v203
	v_mov_b32_e32 v184, v133
	v_cvt_pk_fp8_f32 v184, v185, v188
	v_mul_f32_e32 v190, 0x42800000, v209
	v_mul_f32_e32 v191, 0x42800000, v211
	v_mov_b32_e32 v185, v133
	v_cvt_pk_fp8_f32 v185, v190, v191
	v_mul_f32_e32 v188, 0x42800000, v205
	v_mul_f32_e32 v189, 0x42800000, v207
	v_cvt_pk_fp8_f32 v184, v188, v189 op_sel:[0,0,1]
	v_mul_f32_e32 v188, 0x42800000, v213
	v_mul_f32_e32 v189, 0x42800000, v215
	v_cvt_pk_fp8_f32 v185, v188, v189 op_sel:[0,0,1]
	v_lshl_add_u64 v[188:189], v[186:187], 0, v[140:141]
	global_store_dwordx4 v[188:189], v[178:181], off nt
	s_nop 1
	v_lshl_add_u64 v[178:179], v[186:187], 0, v[142:143]
	global_store_dwordx4 v[178:179], v[182:185], off nt
	s_waitcnt lgkmcnt(0)
	s_cbranch_execz .LBB0_692

; __device__ __forceinline__ void t128_load(const float* W, int N, int item, int lane, f32x4 (&v)[16]) {
;     const int nblk = N / 32, kb = item / nblk, nb = item % nblk, k0 = 128 * kb, n0 = 32 * nb;
; #pragma unroll
;     for (int i = 0; i < 16; ++i) v[i] = __builtin_nontemporal_load((const f32x4*)(W + (size_t)(k0 + i * 8 + (lane >> 3)) * N + n0 + (lane & 7) * 4));
; }
; __device__ __forceinline__ int conv_stream(const Ctx& c, int j, int first, int step, const unsigned* stop, const float* w_gu, const float* w_d, unsigned char* Wgu, unsigned char* Wd) {
;     ...
;         { const int i2 = i + step; const bool more = j + CONV_SLOTS * i2 < CONV_TOTAL && !(stop && stop_poll(c, stop) >= STOP_AT);
;           cs_load(j + CONV_SLOTS * (more ? i2 : i), c.lane, w_gu, w_d, va);
;           cs_store(c, j + CONV_SLOTS * i, vb, Wgu, Wd); i = i2; if (!more) break; }
.LBB0_687:
	s_waitcnt vmcnt(16)
	v_or_b32_e32 v58, s21, v131
	v_ashrrev_i32_e32 v59, 31, v58
	v_lshlrev_b64 v[2:3], s58, v[58:59]
	v_add_u32_e32 v4, 8, v58
	v_add_u32_e32 v10, 16, v58
	v_add_u32_e32 v12, 24, v58
	v_add_u32_e32 v18, 32, v58
	v_add_u32_e32 v20, 40, v58
	v_add_u32_e32 v26, 48, v58
	v_add_u32_e32 v28, 56, v58
	v_add_u32_e32 v34, 64, v58
	v_add_u32_e32 v36, 0x48, v58
	v_add_u32_e32 v42, 0x50, v58
	v_add_u32_e32 v44, 0x58, v58
	v_add_u32_e32 v50, 0x60, v58
	v_add_u32_e32 v52, 0x68, v58
	v_add_u32_e32 v62, 0x70, v58
	v_add_u32_e32 v58, 0x78, v58
	v_ashrrev_i32_e32 v5, 31, v4
	v_ashrrev_i32_e32 v11, 31, v10
	v_ashrrev_i32_e32 v13, 31, v12
	v_ashrrev_i32_e32 v19, 31, v18
	v_ashrrev_i32_e32 v21, 31, v20
	v_ashrrev_i32_e32 v27, 31, v26
	v_ashrrev_i32_e32 v29, 31, v28
	v_ashrrev_i32_e32 v35, 31, v34
	v_ashrrev_i32_e32 v37, 31, v36
	v_ashrrev_i32_e32 v43, 31, v42
	v_ashrrev_i32_e32 v45, 31, v44
	v_ashrrev_i32_e32 v51, 31, v50
	v_ashrrev_i32_e32 v53, 31, v52
	v_ashrrev_i32_e32 v63, 31, v62
	v_ashrrev_i32_e32 v59, 31, v58
	v_lshl_add_u64 v[60:61], s[60:61], 0, v[132:133]
	v_lshlrev_b64 v[4:5], s58, v[4:5]
	v_lshlrev_b64 v[10:11], s58, v[10:11]
	v_lshlrev_b64 v[12:13], s58, v[12:13]
	v_lshlrev_b64 v[18:19], s58, v[18:19]
	v_lshlrev_b64 v[20:21], s58, v[20:21]
	v_lshlrev_b64 v[26:27], s58, v[26:27]
	v_lshlrev_b64 v[28:29], s58, v[28:29]
	v_lshlrev_b64 v[34:35], s58, v[34:35]
	v_lshlrev_b64 v[36:37], s58, v[36:37]
	v_lshlrev_b64 v[42:43], s58, v[42:43]
	v_lshlrev_b64 v[44:45], s58, v[44:45]
	v_lshlrev_b64 v[50:51], s58, v[50:51]
	v_lshlrev_b64 v[52:53], s58, v[52:53]
	v_lshlrev_b64 v[62:63], s58, v[62:63]
	v_lshlrev_b64 v[58:59], s58, v[58:59]
	v_lshl_add_u64 v[2:3], v[60:61], 0, v[2:3]
	v_lshl_add_u64 v[4:5], v[60:61], 0, v[4:5]
	v_lshl_add_u64 v[10:11], v[60:61], 0, v[10:11]
	v_lshl_add_u64 v[12:13], v[60:61], 0, v[12:13]
	v_lshl_add_u64 v[18:19], v[60:61], 0, v[18:19]
	v_lshl_add_u64 v[20:21], v[60:61], 0, v[20:21]
	v_lshl_add_u64 v[26:27], v[60:61], 0, v[26:27]
	v_lshl_add_u64 v[28:29], v[60:61], 0, v[28:29]
	v_lshl_add_u64 v[34:35], v[60:61], 0, v[34:35]
	v_lshl_add_u64 v[36:37], v[60:61], 0, v[36:37]
	v_lshl_add_u64 v[42:43], v[60:61], 0, v[42:43]
	v_lshl_add_u64 v[44:45], v[60:61], 0, v[44:45]
	v_lshl_add_u64 v[50:51], v[60:61], 0, v[50:51]
	v_lshl_add_u64 v[52:53], v[60:61], 0, v[52:53]
	v_lshl_add_u64 v[62:63], v[60:61], 0, v[62:63]
	v_lshl_add_u64 v[58:59], v[60:61], 0, v[58:59]
	s_and_b64 vcc, exec, s[56:57]
	s_cbranch_vccz .Lcv3b_load
	s_waitcnt vmcnt(0)
	s_branch .Lcv3b_noload
.Lcv3b_load:
	global_load_dwordx4 v[6:9], v[2:3], off nt
	s_nop 0
	global_load_dwordx4 v[2:5], v[4:5], off nt
	s_nop 0
	global_load_dwordx4 v[14:17], v[10:11], off nt
	s_nop 0
	global_load_dwordx4 v[10:13], v[12:13], off nt
	s_nop 0
	global_load_dwordx4 v[22:25], v[18:19], off nt
	s_nop 0
	global_load_dwordx4 v[18:21], v[20:21], off nt
	s_nop 0
	global_load_dwordx4 v[30:33], v[26:27], off nt
	s_nop 0
	global_load_dwordx4 v[26:29], v[28:29], off nt
	s_nop 0
	global_load_dwordx4 v[38:41], v[34:35], off nt
	s_nop 0
	global_load_dwordx4 v[34:37], v[36:37], off nt
	s_nop 0
	global_load_dwordx4 v[46:49], v[42:43], off nt
	s_nop 0
	global_load_dwordx4 v[42:45], v[44:45], off nt
	s_nop 0
	global_load_dwordx4 v[54:57], v[50:51], off nt
	s_nop 0
	global_load_dwordx4 v[50:53], v[52:53], off nt
	s_nop 0
	global_load_dwordx4 v[62:65], v[62:63], off nt
	s_nop 0
	global_load_dwordx4 v[58:61], v[58:59], off nt
.Lcv3b_noload:
	s_cmpk_gt_i32 s26, 0x7fff
	s_mov_b64 s[58:59], -1
	s_cbranch_scc0 .LBB0_689
	s_waitcnt vmcnt(31)
	ds_write2_b32 v144, v70, v71 offset1:1
	ds_write2_b32 v144, v72, v73 offset0:2 offset1:3
	s_waitcnt vmcnt(30)
	ds_write2_b32 v149, v66, v67 offset1:1
	ds_write2_b32 v149, v68, v69 offset0:2 offset1:3
	s_waitcnt vmcnt(29)
	ds_write2_b32 v150, v78, v79 offset1:1
	ds_write2_b32 v150, v80, v81 offset0:2 offset1:3
	s_waitcnt vmcnt(28)
	ds_write2_b32 v151, v74, v75 offset1:1
	ds_write2_b32 v151, v76, v77 offset0:2 offset1:3
	s_waitcnt vmcnt(27)
	ds_write2_b32 v154, v86, v87 offset1:1
	ds_write2_b32 v155, v88, v89 offset1:1
	s_waitcnt vmcnt(26)
	ds_write2_b32 v156, v82, v83 offset1:1
	ds_write2_b32 v157, v84, v85 offset1:1
	s_waitcnt vmcnt(25)
	ds_write2_b32 v158, v94, v95 offset1:1
	ds_write2_b32 v159, v96, v97 offset1:1
	s_waitcnt vmcnt(24)
	ds_write2_b32 v160, v90, v91 offset1:1
	ds_write2_b32 v161, v92, v93 offset1:1
	s_waitcnt vmcnt(23)
	ds_write2_b32 v162, v102, v103 offset1:1
	ds_write2_b32 v163, v104, v105 offset1:1
	s_waitcnt vmcnt(22)
	ds_write2_b32 v164, v98, v99 offset1:1
	ds_write2_b32 v165, v100, v101 offset1:1
	s_waitcnt vmcnt(21)
	ds_write2_b32 v166, v110, v111 offset1:1
	ds_write2_b32 v167, v112, v113 offset1:1
	s_waitcnt vmcnt(20)
	ds_write2_b32 v168, v106, v107 offset1:1
	ds_write2_b32 v169, v108, v109 offset1:1
	s_waitcnt vmcnt(19)
	ds_write2_b32 v170, v118, v119 offset1:1
	ds_write2_b32 v171, v120, v121 offset1:1
	s_waitcnt vmcnt(18)
	ds_write2_b32 v172, v114, v115 offset1:1
	ds_write2_b32 v173, v116, v117 offset1:1
	s_waitcnt vmcnt(17)
	ds_write2_b32 v174, v126, v127 offset1:1
	ds_write2_b32 v175, v128, v129 offset1:1
	s_waitcnt vmcnt(16)
	ds_write2_b32 v176, v122, v123 offset1:1
	ds_write2_b32 v177, v124, v125 offset1:1
	s_waitcnt lgkmcnt(0)
	ds_read2_b32 v[182:183], v148 offset1:8
	ds_read2_b32 v[184:185], v148 offset0:33 offset1:41
	ds_read2_b32 v[188:189], v148 offset0:66 offset1:74
	ds_read2_b32 v[190:191], v148 offset0:99 offset1:107
	v_mov_b32_e32 v178, v133
	ds_read2_b32 v[192:193], v148 offset0:132 offset1:140
	ds_read2_b32 v[194:195], v148 offset0:165 offset1:173
	s_waitcnt lgkmcnt(5)
	v_mul_f32_e32 v132, 0x42800000, v182
	s_waitcnt lgkmcnt(4)
; #define LAS __attribute__((address_space(3)))
; #define LDS_WAIT() asm volatile("s_waitcnt lgkmcnt(0)" ::: "memory")
; template <int MODE>
; __device__ __forceinline__ void t128_store(const Ctx& c, const f32x4 (&v)[16], int K, int N, unsigned char* WT, int item) {
;     LAS float* scr = (LAS float*)(c.lds + c.wave * CONV_SCR);
;     const int nblk = N / 32, kb = item / nblk, nb = item % nblk, k0 = 128 * kb, n0 = 32 * nb, lane = c.lane;
; #pragma unroll
;     for (int i = 0; i < 16; ++i) { LAS float* d = scr + (i * 8 + (lane >> 3)) * 33 + (lane & 7) * 4; d[0] = v[i].x; d[1] = v[i].y; d[2] = v[i].z; d[3] = v[i].w; }
;     LDS_WAIT(); asm volatile("" ::: "memory");
;     const int cc = lane & 7;
; #pragma unroll
;     for (int j = 0; j < 4; ++j) { const int n = (lane >> 3) + 8 * j; const LAS float* s = scr + (16 * cc) * 33 + n; int w[4];
; #pragma unroll
;         for (int q = 0; q < 4; ++q) { int t = 0; t = __builtin_amdgcn_cvt_pk_fp8_f32(s[(4 * q) * 33] * WSCALE, s[(4 * q + 1) * 33] * WSCALE, t, false);
;             t = __builtin_amdgcn_cvt_pk_fp8_f32(s[(4 * q + 2) * 33] * WSCALE, s[(4 * q + 3) * 33] * WSCALE, t, true); w[q] = t; }
;         const int dr = drow_of<MODE>(n0 + n);
;         __builtin_nontemporal_store((u32x4){(unsigned)w[0], (unsigned)w[1], (unsigned)w[2], (unsigned)w[3]}, (u32x4*)(WT + (size_t)dr * K + k0 + 16 * cc)); }
;     LDS_WAIT(); asm volatile("" ::: "memory");
; }
; __device__ __forceinline__ void cs_store(const Ctx& c, int it, const f32x4 (&v)[16], unsigned char* Wgu, unsigned char* Wd) {
;     if (it < I_D) { constexpr int per = (DFF / 128) * (D / 32); t128_store<0>(c, v, DFF, D, Wd + (size_t)(it / per) * D * DFF, it % per); }
;     else { const int r = it - I_D; constexpr int per = (D / 128) * (4096 / 32); t128_store<1>(c, v, D, 4096, Wgu + (size_t)(r / per) * 4096 * D, r % per); }
	v_mul_f32_e32 v179, 0x42800000, v184
	v_cvt_pk_fp8_f32 v178, v132, v179
	s_waitcnt lgkmcnt(3)
	v_mul_f32_e32 v132, 0x42800000, v188
	s_waitcnt lgkmcnt(2)
	v_mul_f32_e32 v179, 0x42800000, v190
	ds_read2_b32 v[196:197], v148 offset0:198 offset1:206
	ds_read2_b32 v[198:199], v148 offset0:231 offset1:239
	v_cvt_pk_fp8_f32 v178, v132, v179 op_sel:[0,0,1]
	s_waitcnt lgkmcnt(3)
	v_mul_f32_e32 v132, 0x42800000, v192
	s_waitcnt lgkmcnt(2)
	v_mul_f32_e32 v180, 0x42800000, v194
	v_mov_b32_e32 v179, v133
	ds_read2_b32 v[200:201], v153 offset0:8 offset1:16
	ds_read2_b32 v[202:203], v153 offset0:41 offset1:49
	v_cvt_pk_fp8_f32 v179, v132, v180
	ds_read2_b32 v[204:205], v153 offset0:74 offset1:82
	ds_read2_b32 v[206:207], v153 offset0:107 offset1:115
	ds_read2_b32 v[208:209], v153 offset0:140 offset1:148
	ds_read2_b32 v[210:211], v153 offset0:173 offset1:181
	s_waitcnt lgkmcnt(7)
	v_mul_f32_e32 v132, 0x42800000, v196
	s_waitcnt lgkmcnt(6)
	v_mul_f32_e32 v180, 0x42800000, v198
	v_cvt_pk_fp8_f32 v179, v132, v180 op_sel:[0,0,1]
	s_waitcnt lgkmcnt(5)
	v_mul_f32_e32 v132, 0x42800000, v200
	s_waitcnt lgkmcnt(4)
	v_mul_f32_e32 v181, 0x42800000, v202
	v_mov_b32_e32 v180, v133
	ds_read2_b32 v[212:213], v153 offset0:206 offset1:214
	ds_read2_b32 v[214:215], v153 offset0:239 offset1:247
	v_cvt_pk_fp8_f32 v180, v132, v181
	s_waitcnt lgkmcnt(3)
	v_mul_f32_e32 v184, 0x42800000, v208
	s_waitcnt lgkmcnt(2)
	v_mul_f32_e32 v188, 0x42800000, v210
	v_mov_b32_e32 v181, v133
	v_cvt_pk_fp8_f32 v181, v184, v188
	v_mul_f32_e32 v132, 0x42800000, v204
	v_mul_f32_e32 v182, 0x42800000, v206
	v_cvt_pk_fp8_f32 v180, v132, v182 op_sel:[0,0,1]
	s_waitcnt lgkmcnt(1)
	v_mul_f32_e32 v132, 0x42800000, v212
	s_waitcnt lgkmcnt(0)
	v_mul_f32_e32 v182, 0x42800000, v214
	v_cvt_pk_fp8_f32 v181, v132, v182 op_sel:[0,0,1]
	v_mul_f32_e32 v132, 0x42800000, v183
	v_mul_f32_e32 v183, 0x42800000, v185
	v_mov_b32_e32 v182, v133
	v_cvt_pk_fp8_f32 v182, v132, v183
	v_mul_f32_e32 v185, 0x42800000, v193
	v_mul_f32_e32 v188, 0x42800000, v195
	v_mov_b32_e32 v183, v133
	v_cvt_pk_fp8_f32 v183, v185, v188
	v_mul_f32_e32 v132, 0x42800000, v189
	v_mul_f32_e32 v184, 0x42800000, v191
	v_cvt_pk_fp8_f32 v182, v132, v184 op_sel:[0,0,1]
	v_mul_f32_e32 v132, 0x42800000, v197
	v_mul_f32_e32 v184, 0x42800000, v199
	s_add_i32 s20, s25, 0xffff7c00
	v_cvt_pk_fp8_f32 v183, v132, v184 op_sel:[0,0,1]
	v_mul_f32_e32 v132, 0x42800000, v201
	v_mul_f32_e32 v185, 0x42800000, v203
	v_mov_b32_e32 v184, v133
	s_lshr_b32 s54, s20, 11
	v_cvt_pk_fp8_f32 v184, v132, v185
	v_mul_f32_e32 v189, 0x42800000, v209
	v_mul_f32_e32 v190, 0x42800000, v211
	v_mov_b32_e32 v185, v133
	s_lshl_b64 s[20:21], s[54:55], 23
	v_cvt_pk_fp8_f32 v185, v189, v190
	s_add_u32 s20, s14, s20
	s_addc_u32 s21, s15, s21
	s_and_b32 s27, s26, 0x780
	v_mul_f32_e32 v132, 0x42800000, v205
	v_mul_f32_e32 v188, 0x42800000, v207
	s_add_u32 s20, s20, s27
	v_cvt_pk_fp8_f32 v184, v132, v188 op_sel:[0,0,1]
	v_mul_f32_e32 v132, 0x42800000, v213
	v_mul_f32_e32 v188, 0x42800000, v215
	s_addc_u32 s21, s21, 0
	v_cvt_pk_fp8_f32 v185, v132, v188 op_sel:[0,0,1]
	v_lshl_add_u64 v[186:187], s[20:21], 0, v[134:135]
	ds_read2_b32 v[188:189], v148 offset0:16 offset1:24
	ds_read2_b32 v[190:191], v148 offset0:49 offset1:57
	v_lshl_add_u64 v[216:217], v[186:187], 0, v[136:137]
	global_store_dwordx4 v[216:217], v[178:181], off nt
	s_mov_b64 s[58:59], 0
	s_waitcnt lgkmcnt(1)
	v_mul_f32_e32 v132, 0x42800000, v188
	v_lshl_add_u64 v[178:179], v[186:187], 0, v[138:139]
	global_store_dwordx4 v[178:179], v[182:185], off nt
	ds_read2_b32 v[182:183], v148 offset0:82 offset1:90
	ds_read2_b32 v[184:185], v148 offset0:115 offset1:123
	s_waitcnt lgkmcnt(2)
	v_mul_f32_e32 v179, 0x42800000, v190
	v_mov_b32_e32 v178, v133
	ds_read2_b32 v[192:193], v148 offset0:148 offset1:156
	ds_read2_b32 v[194:195], v148 offset0:181 offset1:189
	v_cvt_pk_fp8_f32 v178, v132, v179
	s_waitcnt lgkmcnt(3)
	v_mul_f32_e32 v132, 0x42800000, v182
	s_waitcnt lgkmcnt(2)
	v_mul_f32_e32 v179, 0x42800000, v184
	ds_read2_b32 v[196:197], v148 offset0:214 offset1:222
	ds_read2_b32 v[198:199], v148 offset0:247 offset1:255
	v_cvt_pk_fp8_f32 v178, v132, v179 op_sel:[0,0,1]
	s_waitcnt lgkmcnt(3)
	v_mul_f32_e32 v132, 0x42800000, v192
	s_waitcnt lgkmcnt(2)
	v_mul_f32_e32 v180, 0x42800000, v194
	v_mov_b32_e32 v179, v133
	ds_read2_b32 v[200:201], v153 offset0:24 offset1:32
	ds_read2_b32 v[202:203], v153 offset0:57 offset1:65
	v_cvt_pk_fp8_f32 v179, v132, v180
	ds_read2_b32 v[204:205], v153 offset0:90 offset1:98
	ds_read2_b32 v[206:207], v153 offset0:123 offset1:131
	ds_read2_b32 v[208:209], v153 offset0:156 offset1:164
	ds_read2_b32 v[210:211], v153 offset0:189 offset1:197
	s_waitcnt lgkmcnt(7)
	v_mul_f32_e32 v132, 0x42800000, v196
	s_waitcnt lgkmcnt(6)
	v_mul_f32_e32 v180, 0x42800000, v198
	v_cvt_pk_fp8_f32 v179, v132, v180 op_sel:[0,0,1]
	s_waitcnt lgkmcnt(5)
	v_mul_f32_e32 v132, 0x42800000, v200
	s_waitcnt lgkmcnt(4)
	v_mul_f32_e32 v181, 0x42800000, v202
	v_mov_b32_e32 v180, v133
	ds_read2_b32 v[212:213], v153 offset0:222 offset1:230
	ds_read2_b32 v[214:215], v152 offset0:127 offset1:135
	v_cvt_pk_fp8_f32 v180, v132, v181
	s_waitcnt lgkmcnt(3)
	v_mul_f32_e32 v184, 0x42800000, v208
	s_waitcnt lgkmcnt(2)
	v_mul_f32_e32 v188, 0x42800000, v210
	v_mov_b32_e32 v181, v133
	v_cvt_pk_fp8_f32 v181, v184, v188
	v_mul_f32_e32 v132, 0x42800000, v204
	v_mul_f32_e32 v182, 0x42800000, v206
	v_cvt_pk_fp8_f32 v180, v132, v182 op_sel:[0,0,1]
	s_waitcnt lgkmcnt(1)
	v_mul_f32_e32 v132, 0x42800000, v212
	s_waitcnt lgkmcnt(0)
	v_mul_f32_e32 v182, 0x42800000, v214
	v_cvt_pk_fp8_f32 v181, v132, v182 op_sel:[0,0,1]
	v_mul_f32_e32 v132, 0x42800000, v189
	v_mul_f32_e32 v184, 0x42800000, v191
	v_mov_b32_e32 v182, v133
	v_cvt_pk_fp8_f32 v182, v132, v184
	v_mul_f32_e32 v132, 0x42800000, v183
	v_mul_f32_e32 v184, 0x42800000, v185
	v_mul_f32_e32 v185, 0x42800000, v193
	v_mul_f32_e32 v188, 0x42800000, v195
	v_mov_b32_e32 v183, v133
	v_cvt_pk_fp8_f32 v183, v185, v188
	v_cvt_pk_fp8_f32 v182, v132, v184 op_sel:[0,0,1]
	v_mul_f32_e32 v132, 0x42800000, v197
	v_mul_f32_e32 v184, 0x42800000, v199
	v_cvt_pk_fp8_f32 v183, v132, v184 op_sel:[0,0,1]
	v_mul_f32_e32 v132, 0x42800000, v201
	v_mul_f32_e32 v185, 0x42800000, v203
	v_mov_b32_e32 v184, v133
	v_cvt_pk_fp8_f32 v184, v132, v185
	v_mul_f32_e32 v189, 0x42800000, v209
	v_mul_f32_e32 v190, 0x42800000, v211
	v_mov_b32_e32 v185, v133
	v_cvt_pk_fp8_f32 v185, v189, v190
	v_mul_f32_e32 v132, 0x42800000, v205
	v_mul_f32_e32 v188, 0x42800000, v207
	v_cvt_pk_fp8_f32 v184, v132, v188 op_sel:[0,0,1]
	v_mul_f32_e32 v132, 0x42800000, v213
	v_mul_f32_e32 v188, 0x42800000, v215
	v_cvt_pk_fp8_f32 v185, v132, v188 op_sel:[0,0,1]
	v_lshl_add_u64 v[188:189], v[186:187], 0, v[140:141]
	global_store_dwordx4 v[188:189], v[178:181], off nt
	s_nop 1
	v_lshl_add_u64 v[178:179], v[186:187], 0, v[142:143]
	global_store_dwordx4 v[178:179], v[182:185], off nt
	s_waitcnt lgkmcnt(0)
